# code placement: merge / W_out / MoE1 moved back to the baseline byte phase mod 8 (one pad nop in cold code), MoE2 kept
# speedup vs baseline: 1.0037x; 1.0037x over previous
.Lcvt_post:
	s_nop 0
	s_mov_b64 exec, -1
	s_waitcnt lgkmcnt(0)
	s_cmp_lg_u32 s92, 0x100
	s_cbranch_scc1 .Lcvt_ret
	v_lshrrev_b32_e32 v2, 6, v0
	v_and_b32_e32 v3, 63, v0
	s_nop 0
	v_readfirstlane_b32 s25, v2
	s_nop 3
	v_lshrrev_b32_e32 v4, 3, v3
	v_and_b32_e32 v5, 7, v3
	v_mul_u32_u24_e32 v7, 17, v4
	v_and_b32_e32 v8, 3, v3
	v_lshl_add_u32 v7, v8, 2, v7
	v_lshlrev_b32_e32 v7, 2, v7
	v_mul_u32_u24_e32 v8, 0x110, v5
	v_add_lshl_u32 v8, v8, v4, 2
	s_mul_i32 s17, s25, 0x2200
	v_add_u32_e32 v7, s17, v7
	v_add_u32_e32 v8, s17, v8
	v_lshlrev_b32_e32 v9, 10, v4
	v_lshl_add_u32 v9, v5, 4, v9
	v_add_u32_e32 v10, 0x2000, v9
	s_cmp_eq_u32 s31, 5
	s_cbranch_scc0 .Lcvt_t3
	s_cmp_ge_u32 s62, 3
	s_cbranch_scc1 .Lcvt_ret
	s_sub_i32 s27, s80, 16
	s_cmp_lt_i32 s27, 0
	s_cbranch_scc1 .Lcvt_ret
	s_mov_b32 s26, 3
	s_movk_i32 s30, 0
	s_movk_i32 s4, 5040
	s_mov_b32 s24, s62
	s_branch .Lcvt_go

.LBB0_1342:
	s_or_b64 exec, exec, s[2:3]
	s_nop 0
	s_waitcnt lgkmcnt(0)
	v_mov_b32_e32 v2, v0
	s_load_dwordx2 s[16:17], s[0:1], 0x100
	s_mov_b32 s2, s92
	s_mov_b32 s3, s63
	s_mov_b32 s24, s59
	s_mov_b32 s4, s80
	s_mov_b32 s18, s62
	s_waitcnt lgkmcnt(0)
	s_barrier
	s_ashr_i32 s19, s18, 31
	s_add_u32 s39, s16, 0x5ca00000
	s_addc_u32 s40, s17, 0
	s_lshl_b64 s[2:3], s[18:19], 25
	s_add_u32 s2, s16, s2
	s_addc_u32 s3, s17, s3
	s_add_u32 s41, s2, 0x26000000
	s_addc_u32 s42, s3, 0
	s_add_u32 s43, s16, 0x600000
	s_addc_u32 s44, s17, 0
	s_add_i32 s45, s24, 0x21900
	s_mov_b64 s[2:3], s[0:1]
	v_mov_b32_e32 v10, v0
	v_mov_b32_e32 v2, s45
	s_load_dwordx2 s[20:21], s[2:3], 0xf0
	ds_read_b128 v[2:5], v2
	v_readfirstlane_b32 s25, v10
	s_waitcnt lgkmcnt(0)
	v_readfirstlane_b32 s6, v2
	s_cmp_gt_i32 s6, -1
	s_cselect_b64 s[12:13], -1, 0
	v_readfirstlane_b32 s14, v3
	v_readfirstlane_b32 s3, v4
	v_readfirstlane_b32 s22, v5
	s_and_b64 vcc, exec, s[12:13]
	s_cbranch_vccz .LBB0_1344
	s_ashr_i32 s23, s22, 31
	s_ashr_i32 s2, s3, 16
	s_and_b32 s92, s3, 0xffff
	s_lshl_b64 s[4:5], s[22:23], 2
	s_add_u32 s4, s43, s4
	s_addc_u32 s5, s44, s5
	s_ashr_i32 s15, s14, 31
	s_lshl_b64 s[8:9], s[14:15], 18
	s_add_u32 s8, s39, s8
	s_mov_b32 s7, s59
	s_addc_u32 s9, s40, s9
	s_lshl_b64 s[10:11], s[6:7], 20
	s_add_u32 s7, s41, s10
	s_addc_u32 s14, s42, s11
	s_ashr_i32 s3, s2, 31
	s_lshl_b64 s[10:11], s[2:3], 18
	s_add_u32 s10, s7, s10
	s_addc_u32 s11, s14, s11
